# speedup vs baseline: 1.0016x; 1.0016x over previous
.Lfc_epi:
	s_nop 7
	v_and_b32_e32 v16, 63, v0
	v_and_b32_e32 v17, 15, v0
	v_lshrrev_b32_e32 v18, 4, v16
	s_lshl_b32 s90, s18, 8
	s_lshl_b32 s91, s17, 7
	s_add_u32 s90, s90, s91
	v_add_u32_e32 v1, s90, v17
	v_lshlrev_b32_e32 v1, 5, v1
	v_lshl_add_u32 v1, v18, 4, v1
	v_lshlrev_b32_e32 v2, 4, v16
	v_add_u32_e32 v2, 0x10000, v2
	v_cmp_gt_u32_e32 vcc, 2, v18
	s_nop 1
	v_cndmask_b32_e32 v1, v2, v1, vcc
	v_cvt_pk_f16_f32 v20, v64, v65
	v_cvt_pk_f16_f32 v21, v66, v67
	v_cvt_pk_f16_f32 v22, v68, v69
	v_cvt_pk_f16_f32 v23, v70, v71
	v_pk_max_f16 v20, v20, 0
	v_pk_max_f16 v21, v21, 0
	v_pk_max_f16 v22, v22, 0
	v_pk_max_f16 v23, v23, 0
	s_nop 1
	v_mfma_f32_16x16x32_f16 v[28:31], v[12:15], v[20:23], 0
	v_cvt_pk_f16_f32 v24, v72, v73
	v_cvt_pk_f16_f32 v25, v74, v75
	v_cvt_pk_f16_f32 v26, v76, v77
	v_cvt_pk_f16_f32 v27, v78, v79
	v_pk_max_f16 v24, v24, 0
	v_pk_max_f16 v25, v25, 0
	v_pk_max_f16 v26, v26, 0
	v_pk_max_f16 v27, v27, 0
	s_nop 1
	v_mfma_f32_16x16x32_f16 v[28:31], v[60:63], v[24:27], v[28:31]
	v_cvt_pk_f16_f32 v20, v80, v81
	v_cvt_pk_f16_f32 v21, v82, v83
	v_cvt_pk_f16_f32 v22, v84, v85
	v_cvt_pk_f16_f32 v23, v86, v87
	v_pk_max_f16 v20, v20, 0
	v_pk_max_f16 v21, v21, 0
	v_pk_max_f16 v22, v22, 0
	v_pk_max_f16 v23, v23, 0
	s_nop 1
	v_mfma_f32_16x16x32_f16 v[28:31], v[56:59], v[20:23], v[28:31]
	v_cvt_pk_f16_f32 v24, v88, v89
	v_cvt_pk_f16_f32 v25, v90, v91
	v_cvt_pk_f16_f32 v26, v92, v93
	v_cvt_pk_f16_f32 v27, v94, v95
	v_pk_max_f16 v24, v24, 0
	v_pk_max_f16 v25, v25, 0
	v_pk_max_f16 v26, v26, 0
	v_pk_max_f16 v27, v27, 0
	s_nop 1
	v_mfma_f32_16x16x32_f16 v[32:35], v[12:15], v[24:27], 0
	v_cvt_pk_f16_f32 v20, v96, v97
	v_cvt_pk_f16_f32 v21, v98, v99
	v_cvt_pk_f16_f32 v22, v100, v101
	v_cvt_pk_f16_f32 v23, v102, v103
	v_pk_max_f16 v20, v20, 0
	v_pk_max_f16 v21, v21, 0
	v_pk_max_f16 v22, v22, 0
	v_pk_max_f16 v23, v23, 0
	s_nop 1
	v_mfma_f32_16x16x32_f16 v[32:35], v[60:63], v[20:23], v[32:35]
	ds_write_b128 v1, v[28:31] offset:0
	v_cvt_pk_f16_f32 v24, v104, v105
	v_cvt_pk_f16_f32 v25, v106, v107
	v_cvt_pk_f16_f32 v26, v108, v109
	v_cvt_pk_f16_f32 v27, v110, v111
	v_pk_max_f16 v24, v24, 0
	v_pk_max_f16 v25, v25, 0
	v_pk_max_f16 v26, v26, 0
	v_pk_max_f16 v27, v27, 0
	s_nop 1
	v_mfma_f32_16x16x32_f16 v[32:35], v[56:59], v[24:27], v[32:35]
	v_cvt_pk_f16_f32 v20, v112, v113
	v_cvt_pk_f16_f32 v21, v114, v115
	v_cvt_pk_f16_f32 v22, v116, v117
	v_cvt_pk_f16_f32 v23, v118, v119
	v_pk_max_f16 v20, v20, 0
	v_pk_max_f16 v21, v21, 0
	v_pk_max_f16 v22, v22, 0
	v_pk_max_f16 v23, v23, 0
	s_nop 1
	v_mfma_f32_16x16x32_f16 v[28:31], v[12:15], v[20:23], 0
	v_cvt_pk_f16_f32 v24, v120, v121
	v_cvt_pk_f16_f32 v25, v122, v123
	v_cvt_pk_f16_f32 v26, v124, v125
	v_cvt_pk_f16_f32 v27, v126, v127
	v_pk_max_f16 v24, v24, 0
	v_pk_max_f16 v25, v25, 0
	v_pk_max_f16 v26, v26, 0
	v_pk_max_f16 v27, v27, 0
	s_nop 1
	v_mfma_f32_16x16x32_f16 v[28:31], v[60:63], v[24:27], v[28:31]
	ds_write_b128 v1, v[32:35] offset:512
	v_cvt_pk_f16_f32 v20, v128, v129
	v_cvt_pk_f16_f32 v21, v130, v131
	v_cvt_pk_f16_f32 v22, v132, v133
	v_cvt_pk_f16_f32 v23, v134, v135
	v_pk_max_f16 v20, v20, 0
	v_pk_max_f16 v21, v21, 0
	v_pk_max_f16 v22, v22, 0
	v_pk_max_f16 v23, v23, 0
	s_nop 1
	v_mfma_f32_16x16x32_f16 v[28:31], v[56:59], v[20:23], v[28:31]
	v_cvt_pk_f16_f32 v24, v136, v137
	v_cvt_pk_f16_f32 v25, v138, v139
	v_cvt_pk_f16_f32 v26, v140, v141
	v_cvt_pk_f16_f32 v27, v142, v143
	v_pk_max_f16 v24, v24, 0
	v_pk_max_f16 v25, v25, 0
	v_pk_max_f16 v26, v26, 0
	v_pk_max_f16 v27, v27, 0
	s_nop 1
	v_mfma_f32_16x16x32_f16 v[32:35], v[12:15], v[24:27], 0
	v_cvt_pk_f16_f32 v20, v144, v145
	v_cvt_pk_f16_f32 v21, v146, v147
	v_cvt_pk_f16_f32 v22, v148, v149
	v_cvt_pk_f16_f32 v23, v150, v151
	v_pk_max_f16 v20, v20, 0
	v_pk_max_f16 v21, v21, 0
	v_pk_max_f16 v22, v22, 0
	v_pk_max_f16 v23, v23, 0
	s_nop 1
	v_mfma_f32_16x16x32_f16 v[32:35], v[60:63], v[20:23], v[32:35]
	ds_write_b128 v1, v[28:31] offset:1024
	v_cvt_pk_f16_f32 v24, v152, v153
	v_cvt_pk_f16_f32 v25, v154, v155
	v_cvt_pk_f16_f32 v26, v156, v157
	v_cvt_pk_f16_f32 v27, v158, v159
	v_pk_max_f16 v24, v24, 0
	v_pk_max_f16 v25, v25, 0
	v_pk_max_f16 v26, v26, 0
	v_pk_max_f16 v27, v27, 0
	s_nop 1
	v_mfma_f32_16x16x32_f16 v[32:35], v[56:59], v[24:27], v[32:35]
	v_cvt_pk_f16_f32 v20, v160, v161
	v_cvt_pk_f16_f32 v21, v162, v163
	v_cvt_pk_f16_f32 v22, v164, v165
	v_cvt_pk_f16_f32 v23, v166, v167
	v_pk_max_f16 v20, v20, 0
	v_pk_max_f16 v21, v21, 0
	v_pk_max_f16 v22, v22, 0
	v_pk_max_f16 v23, v23, 0
	s_nop 1
	v_mfma_f32_16x16x32_f16 v[28:31], v[12:15], v[20:23], 0
	v_cvt_pk_f16_f32 v24, v168, v169
	v_cvt_pk_f16_f32 v25, v170, v171
	v_cvt_pk_f16_f32 v26, v172, v173
	v_cvt_pk_f16_f32 v27, v174, v175
	v_pk_max_f16 v24, v24, 0
	v_pk_max_f16 v25, v25, 0
	v_pk_max_f16 v26, v26, 0
	v_pk_max_f16 v27, v27, 0
	s_nop 1
	v_mfma_f32_16x16x32_f16 v[28:31], v[60:63], v[24:27], v[28:31]
	ds_write_b128 v1, v[32:35] offset:1536
	v_cvt_pk_f16_f32 v20, v176, v177
	v_cvt_pk_f16_f32 v21, v178, v179
	v_cvt_pk_f16_f32 v22, v180, v181
	v_cvt_pk_f16_f32 v23, v182, v183
	v_pk_max_f16 v20, v20, 0
	v_pk_max_f16 v21, v21, 0
	v_pk_max_f16 v22, v22, 0
	v_pk_max_f16 v23, v23, 0
	s_nop 1
	v_mfma_f32_16x16x32_f16 v[28:31], v[56:59], v[20:23], v[28:31]
	v_cvt_pk_f16_f32 v24, v184, v185
	v_cvt_pk_f16_f32 v25, v186, v187
	v_cvt_pk_f16_f32 v26, v188, v189
	v_cvt_pk_f16_f32 v27, v190, v191
	v_pk_max_f16 v24, v24, 0
	v_pk_max_f16 v25, v25, 0
	v_pk_max_f16 v26, v26, 0
	v_pk_max_f16 v27, v27, 0
	s_nop 1
	v_mfma_f32_16x16x32_f16 v[32:35], v[12:15], v[24:27], 0
	v_cvt_pk_f16_f32 v20, v192, v193
	v_cvt_pk_f16_f32 v21, v194, v195
	v_cvt_pk_f16_f32 v22, v196, v197
	v_cvt_pk_f16_f32 v23, v198, v199
	v_pk_max_f16 v20, v20, 0
	v_pk_max_f16 v21, v21, 0
	v_pk_max_f16 v22, v22, 0
	v_pk_max_f16 v23, v23, 0
	s_nop 1
	v_mfma_f32_16x16x32_f16 v[32:35], v[60:63], v[20:23], v[32:35]
	ds_write_b128 v1, v[28:31] offset:2048
	v_cvt_pk_f16_f32 v24, v200, v201
	v_cvt_pk_f16_f32 v25, v202, v203
	v_cvt_pk_f16_f32 v26, v204, v205
	v_cvt_pk_f16_f32 v27, v206, v207
	v_pk_max_f16 v24, v24, 0
	v_pk_max_f16 v25, v25, 0
	v_pk_max_f16 v26, v26, 0
	v_pk_max_f16 v27, v27, 0
	s_nop 1
	v_mfma_f32_16x16x32_f16 v[32:35], v[56:59], v[24:27], v[32:35]
	v_cvt_pk_f16_f32 v20, v208, v209
	v_cvt_pk_f16_f32 v21, v210, v211
	v_cvt_pk_f16_f32 v22, v212, v213
	v_cvt_pk_f16_f32 v23, v214, v215
	v_pk_max_f16 v20, v20, 0
	v_pk_max_f16 v21, v21, 0
	v_pk_max_f16 v22, v22, 0
	v_pk_max_f16 v23, v23, 0
	s_nop 1
	v_mfma_f32_16x16x32_f16 v[28:31], v[12:15], v[20:23], 0
	v_cvt_pk_f16_f32 v24, v216, v217
	v_cvt_pk_f16_f32 v25, v218, v219
	v_cvt_pk_f16_f32 v26, v220, v221
	v_cvt_pk_f16_f32 v27, v222, v223
	v_pk_max_f16 v24, v24, 0
	v_pk_max_f16 v25, v25, 0
	v_pk_max_f16 v26, v26, 0
	v_pk_max_f16 v27, v27, 0
	s_nop 1
	v_mfma_f32_16x16x32_f16 v[28:31], v[60:63], v[24:27], v[28:31]
	ds_write_b128 v1, v[32:35] offset:2560
	v_cvt_pk_f16_f32 v20, v224, v225
	v_cvt_pk_f16_f32 v21, v226, v227
	v_cvt_pk_f16_f32 v22, v228, v229
	v_cvt_pk_f16_f32 v23, v230, v231
	v_pk_max_f16 v20, v20, 0
	v_pk_max_f16 v21, v21, 0
	v_pk_max_f16 v22, v22, 0
	v_pk_max_f16 v23, v23, 0
	s_nop 1
	v_mfma_f32_16x16x32_f16 v[28:31], v[56:59], v[20:23], v[28:31]
	v_cvt_pk_f16_f32 v24, v232, v233
	v_cvt_pk_f16_f32 v25, v234, v235
	v_cvt_pk_f16_f32 v26, v236, v237
	v_cvt_pk_f16_f32 v27, v238, v239
	v_pk_max_f16 v24, v24, 0
	v_pk_max_f16 v25, v25, 0
	v_pk_max_f16 v26, v26, 0
	v_pk_max_f16 v27, v27, 0
	s_nop 1
	v_mfma_f32_16x16x32_f16 v[32:35], v[12:15], v[24:27], 0
	v_cvt_pk_f16_f32 v20, v240, v241
	v_cvt_pk_f16_f32 v21, v242, v243
	v_cvt_pk_f16_f32 v22, v244, v245
	v_cvt_pk_f16_f32 v23, v246, v247
	v_pk_max_f16 v20, v20, 0
	v_pk_max_f16 v21, v21, 0
	v_pk_max_f16 v22, v22, 0
	v_pk_max_f16 v23, v23, 0
	s_nop 1
	v_mfma_f32_16x16x32_f16 v[32:35], v[60:63], v[20:23], v[32:35]
	ds_write_b128 v1, v[28:31] offset:3072
	v_cvt_pk_f16_f32 v24, v248, v249
	v_cvt_pk_f16_f32 v25, v250, v251
	v_cvt_pk_f16_f32 v26, v252, v253
	v_cvt_pk_f16_f32 v27, v254, v255
	v_pk_max_f16 v24, v24, 0
	v_pk_max_f16 v25, v25, 0
	v_pk_max_f16 v26, v26, 0
	v_pk_max_f16 v27, v27, 0
	s_nop 1
	v_mfma_f32_16x16x32_f16 v[32:35], v[56:59], v[24:27], v[32:35]
	s_nop 7
	s_nop 1
	ds_write_b128 v1, v[32:35] offset:3584
